# HGRN2 scan output tiles transposed in lane quads (DPP) and written with one 8-byte store per tile instead of four 2-byte stores
# speedup vs baseline: 1.0058x; 1.0058x over previous
.LBB0_340:
	s_or_b64 exec, exec, s[14:15]
	s_add_i32 s14, s36, 1
	s_cmpk_lg_i32 s22, 0x7e0
	s_cselect_b32 s15, s14, 0x47
	s_cmp_lt_u32 s15, 8
	s_cselect_b64 vcc, -1, 0
	s_lshl_b32 s15, s15, 5
	v_add_u32_e32 v62, s15, v144
	v_sub_u32_e32 v63, 0x7ff, v62
	v_cndmask_b32_e64 v62, v63, v62, s[0:1]
	v_or_b32_e32 v63, s15, v135
	v_sub_u32_e32 v64, 0xff, v63
	v_cndmask_b32_e64 v63, v64, v63, s[0:1]
	v_add_u32_e32 v62, s35, v62
	v_add_u32_e32 v63, s34, v63
	v_cndmask_b32_e32 v64, v62, v63, vcc
	v_mov_b64_e32 v[62:63], s[96:97]
	v_mad_i64_i32 v[62:63], s[16:17], v64, s2, v[62:63]
	v_lshl_add_u64 v[64:65], v[62:63], 0, v[114:115]
	v_mov_b32_e32 v123, v115
	v_mov_b32_e32 v125, v115
	global_load_dwordx4 v[66:69], v[64:65], off offset:3088
	global_load_dwordx4 v[78:81], v[64:65], off offset:3072
	v_lshl_add_u64 v[64:65], v[62:63], 0, v[122:123]
	v_lshl_add_u64 v[62:63], v[62:63], 0, v[124:125]
	global_load_dwordx4 v[82:85], v[64:65], off offset:16
	global_load_dwordx4 v[86:89], v[64:65], off
	global_load_dwordx4 v[74:77], v[62:63], off
	s_nop 0
	global_load_dwordx4 v[62:65], v[62:63], off offset:16
	s_waitcnt lgkmcnt(0)
	s_barrier
	ds_read_b128 v[90:93], v160 offset:25088
	ds_read_b128 v[94:97], v160 offset:16384
	ds_read_b128 v[98:101], v160 offset:29440
	ds_read_b128 v[102:105], v160 offset:25152
	ds_read_b128 v[106:109], v160 offset:16448
	s_waitcnt lgkmcnt(3)
	v_mfma_f32_16x16x32_bf16 v[94:97], v[90:93], v[94:97], 0
	ds_read_b128 v[110:113], v160 offset:20736
	ds_read_b128 v[126:129], v160 offset:29504
	ds_read_b128 v[130:133], v160 offset:20800
	v_add_u32_e32 v125, 0x9000, v161
	v_add_u32_e32 v123, 0x8000, v161
	s_waitcnt lgkmcnt(2)
	v_mfma_f32_16x16x32_bf16 v[98:101], v[98:101], v[110:113], 0
	v_cvt_pk_bf16_f32 v184, v18, v19
	v_cvt_pk_bf16_f32 v185, v20, v21
	v_cvt_pk_bf16_f32 v186, v22, v23
	v_mfma_f32_16x16x32_bf16 v[94:97], v[102:105], v[106:109], v[94:97]
	ds_read_b128 v[106:109], v160 offset:25216
	ds_read_b128 v[164:167], v160 offset:16512
	v_cvt_pk_bf16_f32 v187, v24, v25
	v_cvt_pk_bf16_f32 v196, v26, v27
	v_mfma_f32_16x16x32_bf16 v[90:93], v[90:93], v[110:113], 0
	v_cvt_pk_bf16_f32 v111, v4, v5
	v_cvt_pk_bf16_f32 v112, v6, v7
	v_cvt_pk_bf16_f32 v113, v8, v9
	s_waitcnt lgkmcnt(2)
	v_mfma_f32_16x16x32_bf16 v[98:101], v[126:129], v[130:133], v[98:101]
	ds_read_b128 v[126:129], v160 offset:29568
	ds_read_b128 v[168:171], v160 offset:25280
	ds_read_b128 v[172:175], v160 offset:16576
	v_cvt_pk_bf16_f32 v197, v28, v29
	v_cvt_pk_bf16_f32 v198, v34, v35
	s_waitcnt lgkmcnt(3)
	v_mfma_f32_16x16x32_bf16 v[94:97], v[106:109], v[164:167], v[94:97]
	ds_read_b128 v[164:167], v160 offset:20864
	ds_read_b128 v[176:179], v160 offset:29632
	ds_read_b128 v[180:183], v160 offset:20928
	v_cvt_pk_bf16_f32 v199, v36, v37
	s_add_i32 s15, s22, 0x100
	v_mfma_f32_16x16x32_bf16 v[90:93], v[102:105], v[130:133], v[90:93]
	s_cmp_lt_u32 s36, 8
	s_cselect_b32 s15, s15, s22
	s_cselect_b32 s16, 0xff, s31
	s_waitcnt lgkmcnt(3)
	v_mfma_f32_16x16x32_bf16 v[94:97], v[168:171], v[172:175], v[94:97]
	v_cvt_pk_bf16_f32 v173, v12, v13
	v_cvt_pk_bf16_f32 v172, v10, v11
	v_cvt_pk_bf16_f32 v174, v14, v15
	s_waitcnt lgkmcnt(2)
	v_mfma_f32_16x16x32_bf16 v[90:93], v[106:109], v[164:167], v[90:93]
	v_cvt_pk_bf16_f32 v175, v16, v17
	s_nop 1
	v_cndmask_b32_e64 v110, v94, 0, s[6:7]
	v_cndmask_b32_e64 v102, v95, 0, s[8:9]
	v_cndmask_b32_e64 v103, v96, 0, s[10:11]
	v_cndmask_b32_e64 v104, v97, 0, s[12:13]
	s_waitcnt lgkmcnt(0)
	v_mfma_f32_16x16x32_bf16 v[94:97], v[168:171], v[180:183], v[90:93]
	s_cselect_b32 s17, s34, s35
	s_add_i32 s22, s22, 32
	s_cmpk_lg_i32 s14, 0x48
	v_cvt_pk_bf16_f32 v90, v110, v102
	v_cvt_pk_bf16_f32 v91, v103, v104
	ds_read_b64_tr_b16 v[102:103], v150
	ds_read_b64_tr_b16 v[104:105], v150 offset:4608
	s_waitcnt lgkmcnt(0)
	ds_read2_b64 v[130:133], v125 offset0:160 offset1:168
	v_mfma_f32_16x16x32_bf16 v[98:101], v[126:129], v[164:167], v[98:101]
	ds_read2_b64 v[126:129], v123 offset0:128 offset1:136
	v_cvt_pk_bf16_f32 v110, v2, v3
	v_mov_b32_e32 v92, v115
	v_mfma_f32_16x16x32_bf16 v[98:101], v[176:179], v[180:183], v[98:101]
	s_waitcnt lgkmcnt(1)
	v_mov_b32_e32 v168, v130
	v_mov_b32_e32 v169, v131
	ds_read2_b64 v[176:179], v123 offset0:140 offset1:144
	ds_read2_b64 v[180:183], v125 offset0:172 offset1:176
	ds_read2_b64 v[188:191], v123 offset0:148 offset1:152
	ds_read2_b64 v[192:195], v125 offset0:180 offset1:184
	ds_read_b64 v[130:131], v161 offset:34016
	ds_read_b128 v[200:203], v146 offset:60928
	ds_read_b64 v[166:167], v162 offset:33792
	ds_read_b64 v[170:171], v162 offset:38144
	ds_read_b64 v[208:209], v161 offset:38368
	ds_read_b64_tr_b16 v[210:211], v151
	ds_read_b64_tr_b16 v[212:213], v151 offset:4608
	s_waitcnt lgkmcnt(0)
	ds_read_b128 v[214:217], v146 offset:60992
	s_waitcnt lgkmcnt(4)
	v_pk_mul_f32 v[4:5], v[4:5], v[202:203]
	v_pk_mul_f32 v[2:3], v[2:3], v[200:201]
	ds_read_b64_tr_b16 v[200:201], v152
	ds_read_b64_tr_b16 v[202:203], v152 offset:4608
	s_waitcnt lgkmcnt(0)
	v_mov_b32_e32 v93, v115
	s_waitcnt lgkmcnt(0)
	v_pk_mul_f32 v[8:9], v[8:9], v[216:217]
	v_mfma_f32_16x16x32_bf16 v[2:5], v[210:213], v[102:105], v[2:5]
	ds_read_b128 v[210:213], v146 offset:61056
	v_pk_mul_f32 v[6:7], v[6:7], v[214:215]
	v_cndmask_b32_e64 v98, v98, 0, s[6:7]
	v_cndmask_b32_e64 v99, v99, 0, s[8:9]
	v_mfma_f32_16x16x32_bf16 v[6:9], v[200:203], v[102:105], v[6:9]
	ds_read_b64_tr_b16 v[200:201], v153
	ds_read_b64_tr_b16 v[202:203], v153 offset:4608
	s_waitcnt lgkmcnt(0)
	s_waitcnt lgkmcnt(0)
	v_pk_mul_f32 v[12:13], v[12:13], v[212:213]
	ds_read_b128 v[212:215], v146 offset:61120
	v_pk_mul_f32 v[10:11], v[10:11], v[210:211]
	v_cndmask_b32_e64 v100, v100, 0, s[10:11]
	v_cndmask_b32_e64 v101, v101, 0, s[12:13]
	v_mfma_f32_16x16x32_bf16 v[10:13], v[200:203], v[102:105], v[10:13]
	ds_read_b64_tr_b16 v[200:201], v154
	ds_read_b64_tr_b16 v[202:203], v154 offset:4608
	s_waitcnt lgkmcnt(0)
	s_waitcnt lgkmcnt(0)
	v_pk_mul_f32 v[16:17], v[16:17], v[214:215]
	v_pk_mul_f32 v[14:15], v[14:15], v[212:213]
	ds_read_b128 v[216:219], v146 offset:61184
	v_cvt_pk_bf16_f32 v94, v94, v95
	v_mfma_f32_16x16x32_bf16 v[14:17], v[200:203], v[102:105], v[14:17]
	ds_read_b64_tr_b16 v[200:201], v155
	ds_read_b64_tr_b16 v[202:203], v155 offset:4608
	s_waitcnt lgkmcnt(0)
	ds_read_b128 v[210:213], v146 offset:61248
	s_waitcnt lgkmcnt(1)
	v_pk_mul_f32 v[20:21], v[20:21], v[218:219]
	v_pk_mul_f32 v[18:19], v[18:19], v[216:217]
	v_cvt_pk_bf16_f32 v95, v96, v97
	v_cvt_pk_bf16_f32 v96, v98, v99
	v_mfma_f32_16x16x32_bf16 v[18:21], v[200:203], v[102:105], v[18:21]
	ds_read_b64_tr_b16 v[200:201], v156
	ds_read_b64_tr_b16 v[202:203], v156 offset:4608
	s_waitcnt lgkmcnt(0)
	s_waitcnt lgkmcnt(0)
	v_pk_mul_f32 v[24:25], v[24:25], v[212:213]
	v_pk_mul_f32 v[22:23], v[22:23], v[210:211]
	ds_read_b128 v[214:217], v146 offset:61312
	v_cvt_pk_bf16_f32 v97, v100, v101
	v_mfma_f32_16x16x32_bf16 v[22:25], v[200:203], v[102:105], v[22:25]
	ds_read_b64_tr_b16 v[200:201], v157
	ds_read_b64_tr_b16 v[202:203], v157 offset:4608
	s_waitcnt lgkmcnt(0)
	ds_read_b128 v[210:213], v146 offset:61376
	v_mov_b32_e32 v164, v126
	v_mov_b32_e32 v165, v127
	v_mfma_f32_16x16x32_bf16 v[106:109], v[90:93], v[102:105], 0
	s_waitcnt lgkmcnt(1)
	v_pk_mul_f32 v[28:29], v[28:29], v[216:217]
	v_pk_mul_f32 v[26:27], v[26:27], v[214:215]
	s_waitcnt lgkmcnt(0)
	v_pk_mul_f32 v[36:37], v[36:37], v[212:213]
	v_pk_mul_f32 v[34:35], v[34:35], v[210:211]
	v_mfma_f32_16x16x32_bf16 v[98:101], v[94:97], v[102:105], 0
	v_mov_b32_e32 v126, v132
	v_mov_b32_e32 v127, v133
	v_mov_b32_e32 v206, v194
	v_mfma_f32_16x16x32_bf16 v[26:29], v[200:203], v[102:105], v[26:29]
	ds_read_b64_tr_b16 v[200:201], v158
	ds_read_b64_tr_b16 v[202:203], v158 offset:4608
	s_waitcnt lgkmcnt(0)
	v_mov_b32_e32 v207, v195
	v_cvt_pk_bf16_f32 v194, v54, v55
	v_mfma_f32_16x16x32_bf16 v[34:37], v[200:203], v[102:105], v[34:37]
	v_mov_b32_e32 v102, v128
	v_mov_b32_e32 v103, v129
	v_mov_b32_e32 v104, v176
	v_mov_b32_e32 v105, v177
	v_mfma_f32_16x16x32_bf16 v[106:109], v[164:167], v[110:113], v[106:109]
	v_mov_b32_e32 v128, v180
	v_mov_b32_e32 v129, v181
	v_cvt_pk_bf16_f32 v181, v44, v45
	v_mfma_f32_16x16x32_bf16 v[98:101], v[168:171], v[110:113], v[98:101]
	v_mov_b32_e32 v110, v178
	v_mov_b32_e32 v111, v179
	v_mov_b32_e32 v112, v188
	v_mov_b32_e32 v113, v189
	v_mfma_f32_16x16x32_bf16 v[102:105], v[102:105], v[172:175], v[106:109]
	v_cvt_pk_bf16_f32 v180, v42, v43
	v_cvt_pk_bf16_f32 v195, v56, v57
	s_mov_b32 s36, s14
	v_mfma_f32_16x16x32_bf16 v[98:101], v[126:129], v[172:175], v[98:101]
	v_mov_b32_e32 v128, v190
	v_mov_b32_e32 v129, v191
	v_mov_b32_e32 v106, v182
	v_mov_b32_e32 v107, v183
	v_mov_b32_e32 v108, v192
	v_mfma_f32_16x16x32_bf16 v[102:105], v[110:113], v[184:187], v[102:105]
	v_mov_b32_e32 v109, v193
	v_cvt_pk_bf16_f32 v182, v46, v47
	v_cvt_pk_bf16_f32 v183, v48, v49
	v_mfma_f32_16x16x32_bf16 v[102:105], v[128:131], v[196:199], v[102:105]
	v_or_b32_e32 v128, s15, v134
	v_cvt_pk_bf16_f32 v192, v50, v51
	v_cvt_pk_bf16_f32 v193, v52, v53
	v_mfma_f32_16x16x32_bf16 v[98:101], v[106:109], v[184:187], v[98:101]
	v_and_b32_e32 v110, 3, v204
	v_or_b32_e32 v111, v128, v110
	v_mfma_f32_16x16x32_bf16 v[98:101], v[206:209], v[196:199], v[98:101]
	v_sub_u32_e32 v112, s16, v111
	v_cndmask_b32_e64 v112, v112, v111, s[0:1]
	v_add_u32_e32 v112, s17, v112
	v_lshlrev_b32_e32 v112, 10, v112
	v_sub_u32_e32 v112, v112, v110
	v_ashrrev_i32_e32 v113, 31, v112
	v_lshl_add_u64 v[106:107], v[112:113], 1, v[120:121]
	v_or_b32_e32 v111, 16, v111
	v_sub_u32_e32 v112, s16, v111
	v_cndmask_b32_e64 v112, v112, v111, s[0:1]
	v_add_u32_e32 v112, s17, v112
	v_lshlrev_b32_e32 v112, 10, v112
	v_sub_u32_e32 v112, v112, v110
	v_ashrrev_i32_e32 v113, 31, v112
	v_lshl_add_u64 v[108:109], v[112:113], 1, v[120:121]
	v_and_b32_e32 v126, 1, v204
	v_and_b32_e32 v127, 2, v204
	v_cmp_eq_u32_e64 s[38:39], 0, v126
	v_cmp_ne_u32_e64 s[40:41], 0, v126
	v_cmp_eq_u32_e64 s[42:43], 0, v127
	v_cmp_ne_u32_e64 s[44:45], 0, v127
	s_nop 3
	s_mov_b64 vcc, s[38:39]
	s_nop 1
	v_cndmask_b32_dpp v126, v103, v102, vcc quad_perm:[1,0,3,2] row_mask:0xf bank_mask:0xf
	v_cndmask_b32_dpp v128, v105, v104, vcc quad_perm:[1,0,3,2] row_mask:0xf bank_mask:0xf
	s_mov_b64 vcc, s[40:41]
	s_nop 1
	v_cndmask_b32_dpp v127, v102, v103, vcc quad_perm:[1,0,3,2] row_mask:0xf bank_mask:0xf
	v_cndmask_b32_dpp v129, v104, v105, vcc quad_perm:[1,0,3,2] row_mask:0xf bank_mask:0xf
	s_mov_b64 vcc, s[42:43]
	s_nop 1
	v_cndmask_b32_dpp v130, v128, v126, vcc quad_perm:[2,3,0,1] row_mask:0xf bank_mask:0xf
	v_cndmask_b32_dpp v131, v129, v127, vcc quad_perm:[2,3,0,1] row_mask:0xf bank_mask:0xf
	s_mov_b64 vcc, s[44:45]
	s_nop 1
	v_cndmask_b32_dpp v132, v126, v128, vcc quad_perm:[2,3,0,1] row_mask:0xf bank_mask:0xf
	v_cndmask_b32_dpp v133, v127, v129, vcc quad_perm:[2,3,0,1] row_mask:0xf bank_mask:0xf
	v_cvt_pk_bf16_f32 v110, v130, v131
	v_cvt_pk_bf16_f32 v111, v132, v133
	s_nop 0
	global_store_dwordx2 v[106:107], v[110:111], off
	s_mov_b64 vcc, s[38:39]
	s_nop 1
	v_cndmask_b32_dpp v126, v99, v98, vcc quad_perm:[1,0,3,2] row_mask:0xf bank_mask:0xf
	v_cndmask_b32_dpp v128, v101, v100, vcc quad_perm:[1,0,3,2] row_mask:0xf bank_mask:0xf
	s_mov_b64 vcc, s[40:41]
	s_nop 1
	v_cndmask_b32_dpp v127, v98, v99, vcc quad_perm:[1,0,3,2] row_mask:0xf bank_mask:0xf
	v_cndmask_b32_dpp v129, v100, v101, vcc quad_perm:[1,0,3,2] row_mask:0xf bank_mask:0xf
	s_mov_b64 vcc, s[42:43]
	s_nop 1
	v_cndmask_b32_dpp v130, v128, v126, vcc quad_perm:[2,3,0,1] row_mask:0xf bank_mask:0xf
	v_cndmask_b32_dpp v131, v129, v127, vcc quad_perm:[2,3,0,1] row_mask:0xf bank_mask:0xf
	s_mov_b64 vcc, s[44:45]
	s_nop 1
	v_cndmask_b32_dpp v132, v126, v128, vcc quad_perm:[2,3,0,1] row_mask:0xf bank_mask:0xf
	v_cndmask_b32_dpp v133, v127, v129, vcc quad_perm:[2,3,0,1] row_mask:0xf bank_mask:0xf
	v_cvt_pk_bf16_f32 v110, v130, v131
	v_cvt_pk_bf16_f32 v111, v132, v133
	s_nop 0
	global_store_dwordx2 v[108:109], v[110:111], off
	ds_read_b64_tr_b16 v[98:99], v159
	ds_read_b64_tr_b16 v[100:101], v159 offset:4608
	s_waitcnt lgkmcnt(0)
	ds_read2_b64 v[168:171], v125 offset0:160 offset1:168
	ds_read2_b64 v[164:167], v123 offset0:128 offset1:136
	ds_read2_b64 v[184:187], v123 offset0:140 offset1:144
	ds_read2_b64 v[188:191], v125 offset0:172 offset1:176
	ds_read2_b64 v[196:199], v123 offset0:148 offset1:152
	ds_read2_b64 v[200:203], v125 offset0:180 offset1:184
	v_mfma_f32_16x16x32_bf16 v[102:105], v[90:93], v[98:101], 0
	s_waitcnt lgkmcnt(5)
	v_mov_b32_e32 v176, v168
	v_mov_b32_e32 v177, v169
	ds_read_b64 v[168:169], v161 offset:34016
	ds_read_b128 v[210:213], v146 offset:60928
	ds_read_b64 v[174:175], v162 offset:33792
	ds_read_b64 v[178:179], v162 offset:38144
	ds_read_b64 v[214:215], v161 offset:38368
	ds_read_b64_tr_b16 v[216:217], v151
	ds_read_b64_tr_b16 v[218:219], v151 offset:4608
	s_waitcnt lgkmcnt(0)
	ds_read_b128 v[220:223], v146 offset:60992
	v_mfma_f32_16x16x32_bf16 v[90:93], v[94:97], v[98:101], 0
	v_cvt_pk_bf16_f32 v94, v30, v31
	v_cvt_pk_bf16_f32 v95, v32, v33
	s_waitcnt lgkmcnt(4)
	v_pk_mul_f32 v[32:33], v[32:33], v[212:213]
	v_pk_mul_f32 v[30:31], v[30:31], v[210:211]
	ds_read_b64_tr_b16 v[210:211], v152
	ds_read_b64_tr_b16 v[212:213], v152 offset:4608
	s_waitcnt lgkmcnt(0)
	v_cvt_pk_bf16_f32 v96, v38, v39
	v_cvt_pk_bf16_f32 v97, v40, v41
	v_mfma_f32_16x16x32_bf16 v[30:33], v[216:219], v[98:101], v[30:33]
	ds_read_b128 v[216:219], v146 offset:61056
	s_waitcnt lgkmcnt(1)
	v_pk_mul_f32 v[40:41], v[40:41], v[222:223]
	v_pk_mul_f32 v[38:39], v[38:39], v[220:221]
	v_mov_b32_e32 v172, v164
	v_mov_b32_e32 v173, v165
	v_mfma_f32_16x16x32_bf16 v[38:41], v[210:213], v[98:101], v[38:41]
	ds_read_b64_tr_b16 v[210:211], v153
	ds_read_b64_tr_b16 v[212:213], v153 offset:4608
	s_waitcnt lgkmcnt(0)
	s_waitcnt lgkmcnt(0)
	v_pk_mul_f32 v[44:45], v[44:45], v[218:219]
	ds_read_b128 v[218:221], v146 offset:61120
	v_pk_mul_f32 v[42:43], v[42:43], v[216:217]
	v_cvt_pk_bf16_f32 v206, v58, v59
	v_cvt_pk_bf16_f32 v207, v60, v61
	v_mfma_f32_16x16x32_bf16 v[42:45], v[210:213], v[98:101], v[42:45]
	ds_read_b64_tr_b16 v[210:211], v154
	ds_read_b64_tr_b16 v[212:213], v154 offset:4608
	s_waitcnt lgkmcnt(0)
	s_waitcnt lgkmcnt(0)
	v_pk_mul_f32 v[48:49], v[48:49], v[220:221]
	v_pk_mul_f32 v[46:47], v[46:47], v[218:219]
	ds_read_b128 v[222:225], v146 offset:61184
	v_cvt_pk_bf16_f32 v208, v70, v71
	v_mfma_f32_16x16x32_bf16 v[46:49], v[210:213], v[98:101], v[46:49]
	ds_read_b64_tr_b16 v[210:211], v155
	ds_read_b64_tr_b16 v[212:213], v155 offset:4608
	s_waitcnt lgkmcnt(0)
	ds_read_b128 v[216:219], v146 offset:61248
	s_waitcnt lgkmcnt(1)
	v_pk_mul_f32 v[52:53], v[52:53], v[224:225]
	v_pk_mul_f32 v[50:51], v[50:51], v[222:223]
	v_cvt_pk_bf16_f32 v209, v72, v73
	v_mfma_f32_16x16x32_bf16 v[102:105], v[172:175], v[94:97], v[102:105]
	s_waitcnt lgkmcnt(0)
	v_pk_mul_f32 v[56:57], v[56:57], v[218:219]
	v_pk_mul_f32 v[54:55], v[54:55], v[216:217]
	v_mov_b32_e32 v164, v170
	v_mfma_f32_16x16x32_bf16 v[50:53], v[210:213], v[98:101], v[50:53]
	ds_read_b64_tr_b16 v[210:211], v156
	ds_read_b64_tr_b16 v[212:213], v156 offset:4608
	s_waitcnt lgkmcnt(0)
	ds_read_b128 v[220:223], v146 offset:61312
	v_mov_b32_e32 v165, v171
	v_mfma_f32_16x16x32_bf16 v[54:57], v[210:213], v[98:101], v[54:57]
	ds_read_b64_tr_b16 v[210:211], v157
	ds_read_b64_tr_b16 v[212:213], v157 offset:4608
	s_waitcnt lgkmcnt(0)
	ds_read_b128 v[216:219], v146 offset:61376
	s_waitcnt lgkmcnt(1)
	v_pk_mul_f32 v[60:61], v[60:61], v[222:223]
	v_pk_mul_f32 v[58:59], v[58:59], v[220:221]
	v_mfma_f32_16x16x32_bf16 v[90:93], v[176:179], v[94:97], v[90:93]
	v_mov_b32_e32 v94, v186
	s_waitcnt lgkmcnt(0)
	v_pk_mul_f32 v[72:73], v[72:73], v[218:219]
	v_pk_mul_f32 v[70:71], v[70:71], v[216:217]
	v_mfma_f32_16x16x32_bf16 v[58:61], v[210:213], v[98:101], v[58:61]
	ds_read_b64_tr_b16 v[210:211], v158
	ds_read_b64_tr_b16 v[212:213], v158 offset:4608
	s_waitcnt lgkmcnt(0)
	v_mov_b32_e32 v95, v187
	v_mov_b32_e32 v96, v196
	v_mfma_f32_16x16x32_bf16 v[70:73], v[210:213], v[98:101], v[70:73]
	v_mov_b32_e32 v98, v166
	v_mov_b32_e32 v99, v167
	v_mov_b32_e32 v100, v184
	v_mov_b32_e32 v101, v185
	v_mov_b32_e32 v166, v188
	v_mov_b32_e32 v167, v189
	v_mfma_f32_16x16x32_bf16 v[98:101], v[98:101], v[180:183], v[102:105]
	v_mov_b32_e32 v97, v197
	s_nop 1
	v_mov_b32_e32 v102, v190
	v_mov_b32_e32 v103, v191
	v_mov_b32_e32 v104, v200
	v_mov_b32_e32 v105, v201
	v_mfma_f32_16x16x32_bf16 v[90:93], v[164:167], v[180:183], v[90:93]
	v_mov_b32_e32 v212, v202
	v_mov_b32_e32 v213, v203
	v_mov_b32_e32 v166, v198
	v_mfma_f32_16x16x32_bf16 v[90:93], v[102:105], v[192:195], v[90:93]
	v_mov_b32_e32 v167, v199
	v_mfma_f32_16x16x32_bf16 v[94:97], v[94:97], v[192:195], v[98:101]
	v_mfma_f32_16x16x32_bf16 v[90:93], v[212:215], v[206:209], v[90:93]
	v_mfma_f32_16x16x32_bf16 v[94:97], v[166:169], v[206:209], v[94:97]
	s_nop 6
	s_mov_b64 vcc, s[38:39]
	s_nop 1
	v_cndmask_b32_dpp v126, v95, v94, vcc quad_perm:[1,0,3,2] row_mask:0xf bank_mask:0xf
	v_cndmask_b32_dpp v128, v97, v96, vcc quad_perm:[1,0,3,2] row_mask:0xf bank_mask:0xf
	s_mov_b64 vcc, s[40:41]
	s_nop 1
	v_cndmask_b32_dpp v127, v94, v95, vcc quad_perm:[1,0,3,2] row_mask:0xf bank_mask:0xf
	v_cndmask_b32_dpp v129, v96, v97, vcc quad_perm:[1,0,3,2] row_mask:0xf bank_mask:0xf
	s_mov_b64 vcc, s[42:43]
	s_nop 1
	v_cndmask_b32_dpp v130, v128, v126, vcc quad_perm:[2,3,0,1] row_mask:0xf bank_mask:0xf
	v_cndmask_b32_dpp v131, v129, v127, vcc quad_perm:[2,3,0,1] row_mask:0xf bank_mask:0xf
	s_mov_b64 vcc, s[44:45]
	s_nop 1
	v_cndmask_b32_dpp v132, v126, v128, vcc quad_perm:[2,3,0,1] row_mask:0xf bank_mask:0xf
	v_cndmask_b32_dpp v133, v127, v129, vcc quad_perm:[2,3,0,1] row_mask:0xf bank_mask:0xf
	v_cvt_pk_bf16_f32 v110, v130, v131
	v_cvt_pk_bf16_f32 v111, v132, v133
	s_nop 0
	global_store_dwordx2 v[106:107], v[110:111], off offset:32
	s_mov_b64 vcc, s[38:39]
	s_nop 1
	v_cndmask_b32_dpp v126, v91, v90, vcc quad_perm:[1,0,3,2] row_mask:0xf bank_mask:0xf
	v_cndmask_b32_dpp v128, v93, v92, vcc quad_perm:[1,0,3,2] row_mask:0xf bank_mask:0xf
	s_mov_b64 vcc, s[40:41]
	s_nop 1
	v_cndmask_b32_dpp v127, v90, v91, vcc quad_perm:[1,0,3,2] row_mask:0xf bank_mask:0xf
	v_cndmask_b32_dpp v129, v92, v93, vcc quad_perm:[1,0,3,2] row_mask:0xf bank_mask:0xf
	s_mov_b64 vcc, s[42:43]
	s_nop 1
	v_cndmask_b32_dpp v130, v128, v126, vcc quad_perm:[2,3,0,1] row_mask:0xf bank_mask:0xf
	v_cndmask_b32_dpp v131, v129, v127, vcc quad_perm:[2,3,0,1] row_mask:0xf bank_mask:0xf
	s_mov_b64 vcc, s[44:45]
	s_nop 1
	v_cndmask_b32_dpp v132, v126, v128, vcc quad_perm:[2,3,0,1] row_mask:0xf bank_mask:0xf
	v_cndmask_b32_dpp v133, v127, v129, vcc quad_perm:[2,3,0,1] row_mask:0xf bank_mask:0xf
	v_cvt_pk_bf16_f32 v110, v130, v131
	v_cvt_pk_bf16_f32 v111, v132, v133
	s_nop 0
	global_store_dwordx2 v[108:109], v[110:111], off offset:32
	s_cbranch_scc0 .LBB0_336
